# G=200, dedicated converters 7296 W1 tiles, GEMM-in epilogues 896 tiles, GEMM1 epilogues 3200
# speedup vs baseline: 1.0045x; 1.0045x over previous
.LBB0_86:
	s_cmp_lt_i32 s50, 2
	s_cselect_b64 s[6:7], -1, 0
	s_and_b64 s[0:1], s[6:7], s[2:3]
	s_andn2_b64 vcc, exec, s[0:1]
	v_writelane_b32 v254, s60, 4
	s_cbranch_vccnz .LBB0_260
	s_mov_b64 s[2:3], s[80:81]
	s_load_dwordx2 s[8:9], s[2:3], 0xa8
	s_cmpk_lg_i32 s56, 0x100
	s_cselect_b32 s0, s56, 0xc8
	s_cmp_ge_i32 s78, s0
	s_mov_b64 s[4:5], -1
	s_cbranch_scc0 .LBB0_145
	s_sub_i32 s1, s78, s0
	s_cmpk_gt_i32 s1, 0x1c7f
	s_cbranch_scc1 .LBB0_144
	s_sub_i32 s20, s56, s0
	s_abs_i32 s4, s20
	v_cvt_f32_u32_e32 v1, s4
	s_load_dwordx2 s[10:11], s[2:3], 0x78
	s_load_dwordx2 s[12:13], s[2:3], 0x88
	s_sub_i32 s2, s20, s1
	s_add_i32 s3, s2, 0x1c7f
	v_rcp_iflag_f32_e32 v1, v1
	s_sub_i32 s2, 0xffffe381, s2
	s_xor_b32 s14, s3, s20
	s_sub_i32 s5, 0, s4
	v_mul_f32_e32 v1, 0x4f7ffffe, v1
	v_cvt_u32_f32_e32 v1, v1
	s_max_i32 s2, s3, s2
	s_ashr_i32 s3, s14, 31
	v_readfirstlane_b32 s14, v1
	s_mul_i32 s5, s5, s14
	s_mul_hi_u32 s5, s14, s5
	s_add_i32 s14, s14, s5
	s_mul_hi_u32 s5, s2, s14
	s_mul_i32 s14, s5, s4
	s_sub_i32 s2, s2, s14
	s_add_i32 s14, s5, 1
	s_sub_i32 s15, s2, s4
	s_cmp_ge_u32 s2, s4
	s_cselect_b32 s5, s14, s5
	s_cselect_b32 s2, s15, s2
	s_add_i32 s14, s5, 1
	s_cmp_ge_u32 s2, s4
	s_cselect_b32 s2, s14, s5
	s_xor_b32 s2, s2, s3
	s_sub_i32 s29, s2, s3
	s_lshl_b32 s21, s29, 2
	s_add_i32 s22, s21, -1
	s_cmp_gt_i32 s29, 0
	s_cselect_b64 s[2:3], -1, 0
	s_and_b64 s[4:5], s[2:3], exec
	s_cselect_b32 s18, 0, s22
	s_ashr_i32 s4, s18, 2
	s_mul_i32 s17, s4, s20
	s_add_i32 s17, s17, s1
	s_cmpk_gt_i32 s17, 0x1fff
	s_mov_b32 s5, 0
	s_cbranch_scc0 .LBB0_91
	s_add_i32 s4, s17, 0xffffe000
	s_lshr_b32 s4, s4, 7
	s_lshl_b64 s[4:5], s[4:5], 24
	s_waitcnt lgkmcnt(0)
	s_add_u32 s14, s12, s4
	s_addc_u32 s15, s13, s5
	s_lshl_b32 s4, s17, 4
	s_and_b32 s26, s4, 0x780
	s_lshl_b32 s4, s17, 8
	s_and_b32 s16, s4, 0x700
	s_mov_b64 s[4:5], 0x800
	s_cbranch_execz .LBB0_92
	s_branch .LBB0_93

.LBB0_160:
	s_add_i32 s89, s59, -1
	s_cmp_lt_u32 s89, 9
	s_cselect_b32 s88, 1, 0
	s_cbranch_scc0 .Lp1c_skip1
	s_mul_i32 s89, s89, 200
	s_add_u32 s89, s89, s78
	s_add_u32 s89, s89, 7296
	s_cmp_lt_u32 s89, 0x2000
	s_cselect_b32 s88, 1, 0
	s_cbranch_scc0 .Lp1c_skip1
	s_lshr_b32 s90, s89, 4
	s_lshl_b32 s90, s90, 21
	s_and_b32 s91, s89, 15
	s_lshl_b32 s92, s91, 10
	s_or_b32 s90, s90, s92
	s_lshl_b32 s92, s57, 7
	s_or_b32 s90, s90, s92
	s_add_u32 s84, s82, s90
	s_addc_u32 s85, s83, 0
	s_lshr_b32 s90, s89, 8
	s_lshl_b32 s90, s90, 23
	s_lshl_b32 s91, s91, 19
	s_or_b32 s90, s90, s91
	s_bfe_u32 s91, s89, 0x40004
	s_lshl_b32 s91, s91, 7
	s_or_b32 s90, s90, s91
	s_lshl_b32 s91, s57, 15
	s_or_b32 s90, s90, s91
	s_add_u32 s90, s90, 0x4ee00000
	s_add_u32 s86, s48, s90
	s_addc_u32 s87, s49, 0
	global_load_dwordx4 v[180:183], v245, s[84:85] nt
	s_add_u32 s84, s84, 0x4000
	s_addc_u32 s85, s85, 0
	global_load_dwordx4 v[184:187], v245, s[84:85] nt
	s_add_u32 s84, s84, 0x4000
	s_addc_u32 s85, s85, 0
	global_load_dwordx4 v[188:191], v245, s[84:85] nt
	s_add_u32 s84, s84, 0x4000
	s_addc_u32 s85, s85, 0
	global_load_dwordx4 v[192:195], v245, s[84:85] nt
	s_add_u32 s84, s84, 0x4000
	s_addc_u32 s85, s85, 0
	global_load_dwordx4 v[196:199], v245, s[84:85] nt
	s_add_u32 s84, s84, 0x4000
	s_addc_u32 s85, s85, 0
	global_load_dwordx4 v[200:203], v245, s[84:85] nt
	s_add_u32 s84, s84, 0x4000
	s_addc_u32 s85, s85, 0
	global_load_dwordx4 v[204:207], v245, s[84:85] nt
	s_add_u32 s84, s84, 0x4000
	s_addc_u32 s85, s85, 0
	global_load_dwordx4 v[208:211], v245, s[84:85] nt
	s_add_u32 s84, s84, 0x4000
	s_addc_u32 s85, s85, 0
	global_load_dwordx4 v[212:215], v245, s[84:85] nt
	s_add_u32 s84, s84, 0x4000
	s_addc_u32 s85, s85, 0
	global_load_dwordx4 v[216:219], v245, s[84:85] nt
	s_add_u32 s84, s84, 0x4000
	s_addc_u32 s85, s85, 0
	global_load_dwordx4 v[220:223], v245, s[84:85] nt
	s_add_u32 s84, s84, 0x4000
	s_addc_u32 s85, s85, 0
	global_load_dwordx4 v[224:227], v245, s[84:85] nt
	s_add_u32 s84, s84, 0x4000
	s_addc_u32 s85, s85, 0
	global_load_dwordx4 v[228:231], v245, s[84:85] nt
	s_add_u32 s84, s84, 0x4000
	s_addc_u32 s85, s85, 0
	global_load_dwordx4 v[232:235], v245, s[84:85] nt
	s_add_u32 s84, s84, 0x4000
	s_addc_u32 s85, s85, 0
	global_load_dwordx4 v[236:239], v245, s[84:85] nt
	s_add_u32 s84, s84, 0x4000
	s_addc_u32 s85, s85, 0
	global_load_dwordx4 v[240:243], v245, s[84:85] nt
